# v14 + GEMM epilogue flat stores of EpiGlaIn / EpiSwiGLU / EpiBf16 issued as global stores
# speedup vs baseline: 1.0029x; 1.0029x over previous
.LBB0_317:
	v_or_b32_e32 v144, 16, v132
	v_lshlrev_b32_e32 v140, 3, v138
	v_ashrrev_i32_e32 v133, 31, v132
	v_ashrrev_i32_e32 v145, 31, v144
	v_ashrrev_i32_e32 v141, 31, v140
	v_lshlrev_b64 v[142:143], 7, v[132:133]
	v_lshlrev_b64 v[144:145], 7, v[144:145]
	v_lshl_add_u64 v[142:143], s[8:9], 0, v[142:143]
	v_lshlrev_b64 v[140:141], 2, v[140:141]
	v_lshl_add_u64 v[144:145], s[8:9], 0, v[144:145]
	v_lshl_add_u64 v[142:143], v[142:143], 0, v[140:141]
	v_lshl_add_u64 v[144:145], v[144:145], 0, v[140:141]
	global_store_dwordx4 v[142:143], v[106:109], off
	global_store_dwordx4 v[142:143], v[110:113], off offset:16
	global_store_dwordx4 v[144:145], v[74:77], off
	global_store_dwordx4 v[144:145], v[78:81], off offset:16
	v_or_b32_e32 v144, 32, v132
	v_ashrrev_i32_e32 v145, 31, v144
	v_lshlrev_b64 v[144:145], 7, v[144:145]
	v_lshl_add_u64 v[144:145], s[8:9], 0, v[144:145]
	v_lshl_add_u64 v[144:145], v[144:145], 0, v[140:141]
	global_store_dwordx4 v[144:145], v[40:43], off
	global_store_dwordx4 v[144:145], v[44:47], off offset:16
	v_or_b32_e32 v144, 48, v132
	v_ashrrev_i32_e32 v145, 31, v144
	v_lshlrev_b64 v[144:145], 7, v[144:145]
	v_lshl_add_u64 v[144:145], s[8:9], 0, v[144:145]
	s_movk_i32 s17, 0x4000
	v_lshl_add_u64 v[140:141], v[144:145], 0, v[140:141]
	s_mov_b64 s[10:11], 0x4000
	v_add_co_u32_e32 v144, vcc, s17, v142
	global_store_dwordx4 v[140:141], v[8:11], off
	global_store_dwordx4 v[140:141], v[12:15], off offset:16
	v_lshl_add_u64 v[140:141], v[142:143], 0, s[10:11]
	v_addc_co_u32_e32 v145, vcc, 0, v143, vcc
	s_mov_b64 s[20:21], 0x4800
	global_store_dwordx4 v[144:145], v[98:101], off
	global_store_dwordx4 v[140:141], v[102:105], off offset:16
	v_lshl_add_u64 v[140:141], v[142:143], 0, s[20:21]
	global_store_dwordx4 v[144:145], v[66:69], off offset:2048
	global_store_dwordx4 v[140:141], v[70:73], off offset:16
	s_mov_b64 s[20:21], 0x5000
	v_add_co_u32_e32 v144, vcc, 0x5000, v142
	v_lshl_add_u64 v[140:141], v[142:143], 0, s[20:21]
	s_nop 0
	v_addc_co_u32_e32 v145, vcc, 0, v143, vcc
	s_mov_b64 s[20:21], 0x5800
	global_store_dwordx4 v[144:145], v[32:35], off
	global_store_dwordx4 v[140:141], v[36:39], off offset:16
	v_lshl_add_u64 v[140:141], v[142:143], 0, s[20:21]
	global_store_dwordx4 v[144:145], v[0:3], off offset:2048
	global_store_dwordx4 v[140:141], v[4:7], off offset:16
	s_cbranch_execnz .LBB0_314
.LBB0_318:
	s_lshl_b32 s17, s60, 8
	s_or_b32 s17, s17, s50
	v_lshl_add_u32 v138, v138, 3, s17
	v_ashrrev_i32_e32 v139, 31, v138
	v_mov_b64_e32 v[140:141], s[6:7]
	s_movk_i32 s10, 0x1800
	v_mad_i64_i32 v[142:143], s[20:21], v132, s10, v[140:141]
	v_lshlrev_b64 v[138:139], 1, v[138:139]
	v_lshl_add_u64 v[142:143], v[142:143], 0, v[138:139]
	v_cvt_pk_bf16_f32 v106, v106, v107
	v_cvt_pk_bf16_f32 v107, v108, v109
	v_cvt_pk_bf16_f32 v108, v110, v111
	v_cvt_pk_bf16_f32 v109, v112, v113
	global_store_dwordx4 v[142:143], v[106:109], off
	v_cvt_pk_bf16_f32 v74, v74, v75
	v_cvt_pk_bf16_f32 v75, v76, v77
	v_cvt_pk_bf16_f32 v106, v124, v125
	v_cvt_pk_bf16_f32 v107, v126, v127
	v_cvt_pk_bf16_f32 v108, v128, v129
	v_cvt_pk_bf16_f32 v109, v130, v131
	global_store_dwordx4 v[142:143], v[106:109], off offset:256
	v_cvt_pk_bf16_f32 v76, v78, v79
	v_cvt_pk_bf16_f32 v77, v80, v81
	v_or_b32_e32 v106, 16, v132
	v_mad_i64_i32 v[106:107], s[20:21], v106, s10, v[140:141]
	v_lshl_add_u64 v[106:107], v[106:107], 0, v[138:139]
	global_store_dwordx4 v[106:107], v[74:77], off
	v_cvt_pk_bf16_f32 v40, v40, v41
	v_cvt_pk_bf16_f32 v41, v42, v43
	v_cvt_pk_bf16_f32 v74, v90, v91
	v_cvt_pk_bf16_f32 v75, v92, v93
	v_cvt_pk_bf16_f32 v76, v94, v95
	v_cvt_pk_bf16_f32 v77, v96, v97
	global_store_dwordx4 v[106:107], v[74:77], off offset:256
	v_cvt_pk_bf16_f32 v42, v44, v45
	v_cvt_pk_bf16_f32 v43, v46, v47
	v_or_b32_e32 v74, 32, v132
	v_mad_i64_i32 v[74:75], s[20:21], v74, s10, v[140:141]
	v_lshl_add_u64 v[74:75], v[74:75], 0, v[138:139]
	global_store_dwordx4 v[74:75], v[40:43], off
	v_cvt_pk_bf16_f32 v8, v8, v9
	v_cvt_pk_bf16_f32 v9, v10, v11
	v_cvt_pk_bf16_f32 v40, v56, v57
	v_cvt_pk_bf16_f32 v41, v58, v59
	v_cvt_pk_bf16_f32 v42, v60, v61
	v_cvt_pk_bf16_f32 v43, v62, v63
	global_store_dwordx4 v[74:75], v[40:43], off offset:256
	v_cvt_pk_bf16_f32 v10, v12, v13
	v_cvt_pk_bf16_f32 v11, v14, v15
	v_or_b32_e32 v40, 48, v132
	v_mad_i64_i32 v[40:41], s[20:21], v40, s10, v[140:141]
	v_lshl_add_u64 v[40:41], v[40:41], 0, v[138:139]
	global_store_dwordx4 v[40:41], v[8:11], off
	v_cvt_pk_bf16_f32 v0, v0, v1
	v_cvt_pk_bf16_f32 v1, v2, v3
	v_cvt_pk_bf16_f32 v8, v24, v25
	v_cvt_pk_bf16_f32 v9, v26, v27
	v_cvt_pk_bf16_f32 v10, v28, v29
	v_cvt_pk_bf16_f32 v11, v30, v31
	global_store_dwordx4 v[40:41], v[8:11], off offset:256
	v_cvt_pk_bf16_f32 v2, v4, v5
	v_cvt_pk_bf16_f32 v3, v6, v7
	v_add_u32_e32 v8, 0x80, v132
	v_mad_i64_i32 v[8:9], s[20:21], v8, s10, v[140:141]
	v_lshl_add_u64 v[12:13], v[8:9], 0, v[138:139]
	v_cvt_pk_bf16_f32 v8, v98, v99
	v_cvt_pk_bf16_f32 v9, v100, v101
	v_cvt_pk_bf16_f32 v10, v102, v103
	v_cvt_pk_bf16_f32 v11, v104, v105
	global_store_dwordx4 v[12:13], v[8:11], off
	s_nop 1
	v_cvt_pk_bf16_f32 v8, v116, v117
	v_cvt_pk_bf16_f32 v9, v118, v119
	v_cvt_pk_bf16_f32 v10, v120, v121
	v_cvt_pk_bf16_f32 v11, v122, v123
	global_store_dwordx4 v[12:13], v[8:11], off offset:256
	s_nop 1
	v_add_u32_e32 v8, 0x90, v132
	v_mad_i64_i32 v[8:9], s[20:21], v8, s10, v[140:141]
	v_lshl_add_u64 v[12:13], v[8:9], 0, v[138:139]
	v_cvt_pk_bf16_f32 v8, v66, v67
	v_cvt_pk_bf16_f32 v9, v68, v69
	v_cvt_pk_bf16_f32 v10, v70, v71
	v_cvt_pk_bf16_f32 v11, v72, v73
	global_store_dwordx4 v[12:13], v[8:11], off
	s_nop 1
	v_cvt_pk_bf16_f32 v8, v82, v83
	v_cvt_pk_bf16_f32 v9, v84, v85
	v_cvt_pk_bf16_f32 v10, v86, v87
	v_cvt_pk_bf16_f32 v11, v88, v89
	global_store_dwordx4 v[12:13], v[8:11], off offset:256
	s_nop 1
	v_add_u32_e32 v8, 0xa0, v132
	v_mad_i64_i32 v[8:9], s[20:21], v8, s10, v[140:141]
	v_lshl_add_u64 v[12:13], v[8:9], 0, v[138:139]
	v_cvt_pk_bf16_f32 v8, v32, v33
	v_cvt_pk_bf16_f32 v9, v34, v35
	v_cvt_pk_bf16_f32 v10, v36, v37
	v_cvt_pk_bf16_f32 v11, v38, v39
	global_store_dwordx4 v[12:13], v[8:11], off
	s_nop 1
	v_cvt_pk_bf16_f32 v8, v48, v49
	v_cvt_pk_bf16_f32 v9, v50, v51
	v_cvt_pk_bf16_f32 v10, v52, v53
	v_cvt_pk_bf16_f32 v11, v54, v55
	global_store_dwordx4 v[12:13], v[8:11], off offset:256
	s_nop 1
	v_add_u32_e32 v8, 0xb0, v132
	v_mad_i64_i32 v[8:9], s[20:21], v8, s10, v[140:141]
	v_lshl_add_u64 v[8:9], v[8:9], 0, v[138:139]
	global_store_dwordx4 v[8:9], v[0:3], off
	s_nop 1
	v_cvt_pk_bf16_f32 v0, v16, v17
	v_cvt_pk_bf16_f32 v1, v18, v19
	v_cvt_pk_bf16_f32 v2, v20, v21
	v_cvt_pk_bf16_f32 v3, v22, v23
	global_store_dwordx4 v[8:9], v[0:3], off offset:256
	s_andn2_b64 vcc, exec, s[0:1]
	s_mov_b64 s[0:1], -1
	s_cbranch_vccnz .LBB0_305

.LBB0_1428:
	s_lshl_b32 s2, s61, 8
	v_mbcnt_lo_u32_b32 v133, -1, 0
	v_mbcnt_hi_u32_b32 v133, -1, v133
	s_add_i32 s2, s2, s49
	v_and_or_b32 v132, v133, 15, s2
	s_lshl_b32 s2, s62, 7
	v_ashrrev_i32_e32 v133, 1, v133
	s_or_b32 s2, s2, s50
	v_and_b32_e32 v133, -8, v133
	v_add_u32_e32 v142, s2, v133
	v_mul_f32_e32 v133, 0xbfb8aa3b, v128
	v_exp_f32_e32 v133, v133
	v_mul_f32_e32 v143, 0xbfb8aa3b, v129
	v_exp_f32_e32 v145, v143
	v_ashrrev_i32_e32 v143, 31, v142
	v_add_f32_e32 v133, 1.0, v133
	v_rcp_f32_e32 v144, v133
	v_add_f32_e32 v133, 1.0, v145
	v_rcp_f32_e32 v145, v133
	v_ashrrev_i32_e32 v133, 31, v132
	v_lshlrev_b64 v[146:147], 11, v[132:133]
	v_mul_f32_e32 v133, 0xbfb8aa3b, v130
	v_pk_mul_f32 v[128:129], v[128:129], v[144:145]
	v_mul_f32_e32 v144, 0xbfb8aa3b, v131
	v_exp_f32_e32 v133, v133
	v_exp_f32_e32 v144, v144
	v_pk_mul_f32 v[124:125], v[128:129], v[124:125]
	v_lshl_add_u64 v[146:147], s[12:13], 0, v[146:147]
	v_add_f32_e32 v128, 1.0, v133
	v_add_f32_e32 v129, 1.0, v144
	v_mul_f32_e32 v133, 0xbfb8aa3b, v116
	v_rcp_f32_e32 v128, v128
	v_rcp_f32_e32 v129, v129
	v_exp_f32_e32 v133, v133
	v_mul_f32_e32 v144, 0xbfb8aa3b, v117
	v_exp_f32_e32 v144, v144
	v_pk_mul_f32 v[128:129], v[130:131], v[128:129]
	v_add_f32_e32 v130, 1.0, v133
	v_mul_f32_e32 v133, 0xbfb8aa3b, v118
	v_add_f32_e32 v131, 1.0, v144
	v_exp_f32_e32 v133, v133
	v_mul_f32_e32 v144, 0xbfb8aa3b, v119
	v_exp_f32_e32 v145, v144
	v_rcp_f32_e32 v130, v130
	v_add_f32_e32 v133, 1.0, v133
	v_rcp_f32_e32 v131, v131
	v_rcp_f32_e32 v144, v133
	v_add_f32_e32 v133, 1.0, v145
	v_rcp_f32_e32 v145, v133
	v_pk_mul_f32 v[116:117], v[116:117], v[130:131]
	v_pk_mul_f32 v[126:127], v[128:129], v[126:127]
	v_pk_mul_f32 v[128:129], v[116:117], v[120:121]
	v_pk_mul_f32 v[116:117], v[118:119], v[144:145]
	v_lshlrev_b64 v[118:119], 1, v[142:143]
	v_pk_mul_f32 v[130:131], v[116:117], v[122:123]
	v_lshl_add_u64 v[116:117], v[146:147], 0, v[118:119]
	v_cvt_pk_bf16_f32 v120, v124, v125
	v_cvt_pk_bf16_f32 v121, v126, v127
	v_cvt_pk_bf16_f32 v122, v128, v129
	v_cvt_pk_bf16_f32 v123, v130, v131
	global_store_dwordx4 v[116:117], v[120:123], off
	s_mov_b32 s2, 0x40000
	s_nop 0
	v_mul_f32_e32 v120, 0xbfb8aa3b, v110
	v_exp_f32_e32 v121, v120
	v_mul_f32_e32 v120, 0xbfb8aa3b, v111
	v_exp_f32_e32 v123, v120
	v_or_b32_e32 v120, 16, v132
	v_add_f32_e32 v121, 1.0, v121
	v_rcp_f32_e32 v122, v121
	v_add_f32_e32 v121, 1.0, v123
	v_rcp_f32_e32 v123, v121
	v_ashrrev_i32_e32 v121, 31, v120
	v_lshlrev_b64 v[120:121], 11, v[120:121]
	v_lshl_add_u64 v[120:121], s[12:13], 0, v[120:121]
	v_pk_mul_f32 v[110:111], v[110:111], v[122:123]
	v_mul_f32_e32 v122, 0xbfb8aa3b, v112
	v_mul_f32_e32 v123, 0xbfb8aa3b, v113
	v_exp_f32_e32 v122, v122
	v_exp_f32_e32 v123, v123
	v_pk_mul_f32 v[106:107], v[110:111], v[106:107]
	v_add_f32_e32 v110, 1.0, v122
	v_add_f32_e32 v111, 1.0, v123
	v_mul_f32_e32 v122, 0xbfb8aa3b, v98
	v_mul_f32_e32 v123, 0xbfb8aa3b, v99
	v_rcp_f32_e32 v110, v110
	v_rcp_f32_e32 v111, v111
	v_exp_f32_e32 v122, v122
	v_exp_f32_e32 v123, v123
	v_pk_mul_f32 v[110:111], v[112:113], v[110:111]
	v_add_f32_e32 v112, 1.0, v122
	v_add_f32_e32 v113, 1.0, v123
	v_mul_f32_e32 v122, 0xbfb8aa3b, v100
	v_mul_f32_e32 v123, 0xbfb8aa3b, v101
	v_exp_f32_e32 v122, v122
	v_exp_f32_e32 v123, v123
	v_rcp_f32_e32 v112, v112
	v_rcp_f32_e32 v113, v113
	v_add_f32_e32 v122, 1.0, v122
	v_add_f32_e32 v123, 1.0, v123
	v_rcp_f32_e32 v122, v122
	v_rcp_f32_e32 v123, v123
	v_pk_mul_f32 v[98:99], v[98:99], v[112:113]
	v_pk_mul_f32 v[108:109], v[110:111], v[108:109]
	v_pk_mul_f32 v[102:103], v[98:99], v[102:103]
	v_pk_mul_f32 v[98:99], v[100:101], v[122:123]
	v_lshl_add_u64 v[110:111], v[120:121], 0, v[118:119]
	v_pk_mul_f32 v[104:105], v[98:99], v[104:105]
	v_cvt_pk_bf16_f32 v98, v106, v107
	v_cvt_pk_bf16_f32 v99, v108, v109
	v_cvt_pk_bf16_f32 v100, v102, v103
	v_cvt_pk_bf16_f32 v101, v104, v105
	global_store_dwordx4 v[110:111], v[98:101], off
	s_nop 1
	v_mul_f32_e32 v98, 0xbfb8aa3b, v94
	v_exp_f32_e32 v99, v98
	v_mul_f32_e32 v98, 0xbfb8aa3b, v95
	v_exp_f32_e32 v101, v98
	v_or_b32_e32 v98, 32, v132
	v_add_f32_e32 v99, 1.0, v99
	v_rcp_f32_e32 v100, v99
	v_add_f32_e32 v99, 1.0, v101
	v_rcp_f32_e32 v101, v99
	v_ashrrev_i32_e32 v99, 31, v98
	v_lshlrev_b64 v[98:99], 11, v[98:99]
	v_lshl_add_u64 v[98:99], s[12:13], 0, v[98:99]
	v_pk_mul_f32 v[94:95], v[94:95], v[100:101]
	v_mul_f32_e32 v100, 0xbfb8aa3b, v96
	v_mul_f32_e32 v101, 0xbfb8aa3b, v97
	v_exp_f32_e32 v100, v100
	v_exp_f32_e32 v101, v101
	v_pk_mul_f32 v[90:91], v[94:95], v[90:91]
	v_add_f32_e32 v94, 1.0, v100
	v_add_f32_e32 v95, 1.0, v101
	v_mul_f32_e32 v100, 0xbfb8aa3b, v82
	v_mul_f32_e32 v101, 0xbfb8aa3b, v83
	v_rcp_f32_e32 v94, v94
	v_rcp_f32_e32 v95, v95
	v_exp_f32_e32 v100, v100
	v_exp_f32_e32 v101, v101
	v_pk_mul_f32 v[94:95], v[96:97], v[94:95]
	v_add_f32_e32 v96, 1.0, v100
	v_add_f32_e32 v97, 1.0, v101
	v_mul_f32_e32 v100, 0xbfb8aa3b, v84
	v_mul_f32_e32 v101, 0xbfb8aa3b, v85
	v_exp_f32_e32 v100, v100
	v_exp_f32_e32 v101, v101
	v_rcp_f32_e32 v96, v96
	v_rcp_f32_e32 v97, v97
	v_add_f32_e32 v100, 1.0, v100
	v_add_f32_e32 v101, 1.0, v101
	v_rcp_f32_e32 v100, v100
	v_rcp_f32_e32 v101, v101
	v_pk_mul_f32 v[82:83], v[82:83], v[96:97]
	v_pk_mul_f32 v[92:93], v[94:95], v[92:93]
	v_pk_mul_f32 v[86:87], v[82:83], v[86:87]
	v_pk_mul_f32 v[82:83], v[84:85], v[100:101]
	v_lshl_add_u64 v[94:95], v[98:99], 0, v[118:119]
	v_pk_mul_f32 v[88:89], v[82:83], v[88:89]
	v_cvt_pk_bf16_f32 v82, v90, v91
	v_cvt_pk_bf16_f32 v83, v92, v93
	v_cvt_pk_bf16_f32 v84, v86, v87
	v_cvt_pk_bf16_f32 v85, v88, v89
	global_store_dwordx4 v[94:95], v[82:85], off
	s_nop 1
	v_mul_f32_e32 v82, 0xbfb8aa3b, v78
	v_exp_f32_e32 v83, v82
	v_mul_f32_e32 v82, 0xbfb8aa3b, v79
	v_exp_f32_e32 v85, v82
	v_or_b32_e32 v82, 48, v132
	v_add_f32_e32 v83, 1.0, v83
	v_rcp_f32_e32 v84, v83
	v_add_f32_e32 v83, 1.0, v85
	v_rcp_f32_e32 v85, v83
	v_ashrrev_i32_e32 v83, 31, v82
	v_lshlrev_b64 v[82:83], 11, v[82:83]
	v_lshl_add_u64 v[82:83], s[12:13], 0, v[82:83]
	v_pk_mul_f32 v[78:79], v[78:79], v[84:85]
	v_mul_f32_e32 v84, 0xbfb8aa3b, v80
	v_mul_f32_e32 v85, 0xbfb8aa3b, v81
	v_exp_f32_e32 v84, v84
	v_exp_f32_e32 v85, v85
	v_pk_mul_f32 v[74:75], v[78:79], v[74:75]
	v_add_f32_e32 v78, 1.0, v84
	v_add_f32_e32 v79, 1.0, v85
	v_mul_f32_e32 v84, 0xbfb8aa3b, v56
	v_mul_f32_e32 v85, 0xbfb8aa3b, v57
	v_rcp_f32_e32 v78, v78
	v_rcp_f32_e32 v79, v79
	v_exp_f32_e32 v84, v84
	v_exp_f32_e32 v85, v85
	v_pk_mul_f32 v[78:79], v[80:81], v[78:79]
	v_add_f32_e32 v80, 1.0, v84
	v_add_f32_e32 v81, 1.0, v85
	v_mul_f32_e32 v84, 0xbfb8aa3b, v58
	v_mul_f32_e32 v85, 0xbfb8aa3b, v59
	v_exp_f32_e32 v84, v84
	v_exp_f32_e32 v85, v85
	v_rcp_f32_e32 v80, v80
	v_rcp_f32_e32 v81, v81
	v_add_f32_e32 v84, 1.0, v84
	v_add_f32_e32 v85, 1.0, v85
	v_rcp_f32_e32 v84, v84
	v_rcp_f32_e32 v85, v85
	v_pk_mul_f32 v[56:57], v[56:57], v[80:81]
	v_pk_mul_f32 v[76:77], v[78:79], v[76:77]
	v_pk_mul_f32 v[70:71], v[56:57], v[70:71]
	v_pk_mul_f32 v[56:57], v[58:59], v[84:85]
	v_lshl_add_u64 v[78:79], v[82:83], 0, v[118:119]
	v_pk_mul_f32 v[72:73], v[56:57], v[72:73]
	v_mul_f32_e32 v57, 0xbfb8aa3b, v66
	v_exp_f32_e32 v58, v57
	v_mul_f32_e32 v57, 0xbfb8aa3b, v67
	v_exp_f32_e32 v59, v57
	v_cvt_pk_bf16_f32 v56, v74, v75
	v_add_f32_e32 v58, 1.0, v58
	v_rcp_f32_e32 v74, v58
	v_add_f32_e32 v58, 1.0, v59
	v_rcp_f32_e32 v75, v58
	v_cvt_pk_bf16_f32 v57, v76, v77
	v_cvt_pk_bf16_f32 v58, v70, v71
	v_cvt_pk_bf16_f32 v59, v72, v73
	global_store_dwordx4 v[78:79], v[56:59], off
	s_nop 1
	v_pk_mul_f32 v[56:57], v[66:67], v[74:75]
	v_mul_f32_e32 v66, 0xbfb8aa3b, v50
	v_pk_mul_f32 v[56:57], v[56:57], v[60:61]
	v_mul_f32_e32 v60, 0xbfb8aa3b, v48
	v_mul_f32_e32 v61, 0xbfb8aa3b, v49
	v_exp_f32_e32 v60, v60
	v_exp_f32_e32 v61, v61
	v_mul_f32_e32 v67, 0xbfb8aa3b, v51
	v_exp_f32_e32 v66, v66
	v_exp_f32_e32 v67, v67
	v_mul_f32_e32 v58, 0xbfb8aa3b, v68
	v_mul_f32_e32 v59, 0xbfb8aa3b, v69
	v_add_f32_e32 v60, 1.0, v60
	v_add_f32_e32 v61, 1.0, v61
	v_exp_f32_e32 v58, v58
	v_exp_f32_e32 v59, v59
	v_rcp_f32_e32 v60, v60
	v_rcp_f32_e32 v61, v61
	v_add_f32_e32 v66, 1.0, v66
	v_add_f32_e32 v67, 1.0, v67
	v_rcp_f32_e32 v66, v66
	v_rcp_f32_e32 v67, v67
	v_add_f32_e32 v58, 1.0, v58
	v_add_f32_e32 v59, 1.0, v59
	v_pk_mul_f32 v[48:49], v[48:49], v[60:61]
	v_rcp_f32_e32 v58, v58
	v_rcp_f32_e32 v59, v59
	v_pk_mul_f32 v[52:53], v[48:49], v[52:53]
	v_pk_mul_f32 v[48:49], v[50:51], v[66:67]
	v_mul_f32_e32 v51, 0xbfb8aa3b, v44
	v_cvt_pk_bf16_f32 v50, v52, v53
	v_exp_f32_e32 v52, v51
	v_mul_f32_e32 v51, 0xbfb8aa3b, v45
	v_exp_f32_e32 v53, v51
	v_pk_mul_f32 v[58:59], v[68:69], v[58:59]
	v_pk_mul_f32 v[54:55], v[48:49], v[54:55]
	v_pk_mul_f32 v[58:59], v[58:59], v[62:63]
	v_cvt_pk_bf16_f32 v51, v54, v55
	v_add_co_u32_e32 v54, vcc, s2, v116
	v_cvt_pk_bf16_f32 v48, v56, v57
	v_cvt_pk_bf16_f32 v49, v58, v59
	v_add_f32_e32 v52, 1.0, v52
	v_add_f32_e32 v53, 1.0, v53
	v_addc_co_u32_e32 v55, vcc, 0, v117, vcc
	v_rcp_f32_e32 v52, v52
	v_rcp_f32_e32 v53, v53
	global_store_dwordx4 v[54:55], v[48:51], off
	s_mov_b32 s2, 0x48000
	v_pk_mul_f32 v[44:45], v[44:45], v[52:53]
	v_mul_f32_e32 v48, 0xbfb8aa3b, v46
	v_mul_f32_e32 v49, 0xbfb8aa3b, v47
	v_exp_f32_e32 v48, v48
	v_exp_f32_e32 v49, v49
	v_pk_mul_f32 v[40:41], v[44:45], v[40:41]
	v_add_f32_e32 v44, 1.0, v48
	v_add_f32_e32 v45, 1.0, v49
	v_mul_f32_e32 v48, 0xbfb8aa3b, v32
	v_mul_f32_e32 v49, 0xbfb8aa3b, v33
	v_rcp_f32_e32 v44, v44
	v_rcp_f32_e32 v45, v45
	v_exp_f32_e32 v48, v48
	v_exp_f32_e32 v49, v49
	v_pk_mul_f32 v[44:45], v[46:47], v[44:45]
	v_add_f32_e32 v46, 1.0, v48
	v_add_f32_e32 v47, 1.0, v49
	v_mul_f32_e32 v48, 0xbfb8aa3b, v34
	v_mul_f32_e32 v49, 0xbfb8aa3b, v35
	v_exp_f32_e32 v48, v48
	v_exp_f32_e32 v49, v49
	v_rcp_f32_e32 v46, v46
	v_rcp_f32_e32 v47, v47
	v_add_f32_e32 v48, 1.0, v48
	v_add_f32_e32 v49, 1.0, v49
	v_rcp_f32_e32 v48, v48
	v_rcp_f32_e32 v49, v49
	v_pk_mul_f32 v[32:33], v[32:33], v[46:47]
	v_pk_mul_f32 v[42:43], v[44:45], v[42:43]
	v_pk_mul_f32 v[36:37], v[32:33], v[36:37]
	v_pk_mul_f32 v[32:33], v[34:35], v[48:49]
	v_mul_f32_e32 v35, 0xbfb8aa3b, v28
	v_cvt_pk_bf16_f32 v34, v36, v37
	v_exp_f32_e32 v36, v35
	v_mul_f32_e32 v35, 0xbfb8aa3b, v29
	v_exp_f32_e32 v37, v35
	v_pk_mul_f32 v[38:39], v[32:33], v[38:39]
	v_cvt_pk_bf16_f32 v32, v40, v41
	v_cvt_pk_bf16_f32 v35, v38, v39
	v_add_co_u32_e32 v38, vcc, s2, v116
	v_cvt_pk_bf16_f32 v33, v42, v43
	v_add_f32_e32 v36, 1.0, v36
	v_add_f32_e32 v37, 1.0, v37
	v_addc_co_u32_e32 v39, vcc, 0, v117, vcc
	v_rcp_f32_e32 v36, v36
	v_rcp_f32_e32 v37, v37
	global_store_dwordx4 v[38:39], v[32:35], off
	s_mov_b32 s2, 0x50000
	v_pk_mul_f32 v[28:29], v[28:29], v[36:37]
	v_mul_f32_e32 v32, 0xbfb8aa3b, v30
	v_mul_f32_e32 v33, 0xbfb8aa3b, v31
	v_exp_f32_e32 v32, v32
	v_exp_f32_e32 v33, v33
	v_pk_mul_f32 v[24:25], v[28:29], v[24:25]
	v_add_f32_e32 v28, 1.0, v32
	v_add_f32_e32 v29, 1.0, v33
	v_mul_f32_e32 v32, 0xbfb8aa3b, v16
	v_mul_f32_e32 v33, 0xbfb8aa3b, v17
	v_rcp_f32_e32 v28, v28
	v_rcp_f32_e32 v29, v29
	v_exp_f32_e32 v32, v32
	v_exp_f32_e32 v33, v33
	v_pk_mul_f32 v[28:29], v[30:31], v[28:29]
	v_add_f32_e32 v30, 1.0, v32
	v_add_f32_e32 v31, 1.0, v33
	v_mul_f32_e32 v32, 0xbfb8aa3b, v18
	v_mul_f32_e32 v33, 0xbfb8aa3b, v19
	v_exp_f32_e32 v32, v32
	v_exp_f32_e32 v33, v33
	v_rcp_f32_e32 v30, v30
	v_rcp_f32_e32 v31, v31
	v_add_f32_e32 v32, 1.0, v32
	v_add_f32_e32 v33, 1.0, v33
	v_rcp_f32_e32 v32, v32
	v_rcp_f32_e32 v33, v33
	v_pk_mul_f32 v[16:17], v[16:17], v[30:31]
	v_pk_mul_f32 v[26:27], v[28:29], v[26:27]
	v_pk_mul_f32 v[20:21], v[16:17], v[20:21]
	v_pk_mul_f32 v[16:17], v[18:19], v[32:33]
	v_mul_f32_e32 v19, 0xbfb8aa3b, v12
	v_cvt_pk_bf16_f32 v18, v20, v21
	v_exp_f32_e32 v20, v19
	v_mul_f32_e32 v19, 0xbfb8aa3b, v13
	v_exp_f32_e32 v21, v19
	v_pk_mul_f32 v[22:23], v[16:17], v[22:23]
	v_cvt_pk_bf16_f32 v16, v24, v25
	v_cvt_pk_bf16_f32 v19, v22, v23
	v_add_co_u32_e32 v22, vcc, s2, v116
	v_cvt_pk_bf16_f32 v17, v26, v27
	v_add_f32_e32 v20, 1.0, v20
	v_add_f32_e32 v21, 1.0, v21
	v_addc_co_u32_e32 v23, vcc, 0, v117, vcc
	v_rcp_f32_e32 v20, v20
	v_rcp_f32_e32 v21, v21
	global_store_dwordx4 v[22:23], v[16:19], off
	v_pk_mul_f32 v[12:13], v[12:13], v[20:21]
	s_nop 0
	v_mul_f32_e32 v16, 0xbfb8aa3b, v14
	v_mul_f32_e32 v17, 0xbfb8aa3b, v15
	v_exp_f32_e32 v16, v16
	v_exp_f32_e32 v17, v17
	v_pk_mul_f32 v[8:9], v[12:13], v[8:9]
	v_add_f32_e32 v12, 1.0, v16
	v_add_f32_e32 v13, 1.0, v17
	v_mul_f32_e32 v16, 0xbfb8aa3b, v0
	v_mul_f32_e32 v17, 0xbfb8aa3b, v1
	v_rcp_f32_e32 v12, v12
	v_rcp_f32_e32 v13, v13
	v_exp_f32_e32 v16, v16
	v_exp_f32_e32 v17, v17
	v_pk_mul_f32 v[12:13], v[14:15], v[12:13]
	v_add_f32_e32 v14, 1.0, v16
	v_add_f32_e32 v15, 1.0, v17
	v_mul_f32_e32 v16, 0xbfb8aa3b, v2
	v_mul_f32_e32 v17, 0xbfb8aa3b, v3
	v_exp_f32_e32 v16, v16
	v_exp_f32_e32 v17, v17
	v_rcp_f32_e32 v14, v14
	v_rcp_f32_e32 v15, v15
	v_add_f32_e32 v16, 1.0, v16
	v_add_f32_e32 v17, 1.0, v17
	v_rcp_f32_e32 v16, v16
	v_rcp_f32_e32 v17, v17
	v_pk_mul_f32 v[0:1], v[0:1], v[14:15]
	v_pk_mul_f32 v[10:11], v[12:13], v[10:11]
	v_pk_mul_f32 v[4:5], v[0:1], v[4:5]
	v_pk_mul_f32 v[0:1], v[2:3], v[16:17]
	v_cvt_pk_bf16_f32 v2, v4, v5
	v_add_co_u32_e32 v4, vcc, 0x58000, v116
	v_pk_mul_f32 v[6:7], v[0:1], v[6:7]
	s_nop 0
	v_addc_co_u32_e32 v5, vcc, 0, v117, vcc
	v_cvt_pk_bf16_f32 v0, v8, v9
	v_cvt_pk_bf16_f32 v1, v10, v11
	v_cvt_pk_bf16_f32 v3, v6, v7
	s_and_b64 vcc, exec, s[0:1]
	s_mov_b64 s[0:1], -1
	global_store_dwordx4 v[4:5], v[0:3], off
	s_cbranch_vccnz .LBB0_1417
	s_andn2_b64 vcc, exec, s[10:11]
	s_cbranch_vccnz .LBB0_1416
	s_barrier
	s_branch .LBB0_1416

.LBB0_1509:
	s_lshl_b32 s4, s20, 8
	v_mbcnt_lo_u32_b32 v132, -1, 0
	v_mbcnt_hi_u32_b32 v132, -1, v132
	s_add_i32 s4, s4, s21
	v_and_or_b32 v136, v132, 15, s4
	s_lshl_b32 s4, s60, 8
	v_ashrrev_i32_e32 v132, 1, v132
	s_or_b32 s4, s4, s50
	v_and_b32_e32 v132, -8, v132
	v_add_u32_e32 v132, s4, v132
	v_ashrrev_i32_e32 v137, 31, v136
	v_ashrrev_i32_e32 v133, 31, v132
	v_lshlrev_b64 v[134:135], 11, v[136:137]
	v_lshl_add_u64 v[134:135], s[8:9], 0, v[134:135]
	v_lshlrev_b64 v[138:139], 1, v[132:133]
	v_lshl_add_u64 v[132:133], v[134:135], 0, v[138:139]
	v_lshl_add_u64 v[134:135], v[136:137], 2, s[2:3]
	global_load_dword v146, v[134:135], off
	global_load_dword v148, v[134:135], off offset:64
	global_load_dword v150, v[134:135], off offset:128
	global_load_dword v152, v[134:135], off offset:192
	global_load_dword v154, v[134:135], off offset:512
	global_load_dword v156, v[134:135], off offset:576
	global_load_dword v158, v[134:135], off offset:640
	global_load_dword v160, v[134:135], off offset:704
	s_mov_b64 s[4:5], 0x40000
	s_waitcnt vmcnt(0) lgkmcnt(0)
	v_pk_mul_f32 v[118:119], v[118:119], v[146:147] op_sel_hi:[1,0]
	v_pk_mul_f32 v[116:117], v[116:117], v[146:147] op_sel_hi:[1,0]
	v_pk_mul_f32 v[122:123], v[122:123], v[146:147] op_sel_hi:[1,0]
	v_pk_mul_f32 v[120:121], v[120:121], v[146:147] op_sel_hi:[1,0]
	v_cvt_pk_bf16_f32 v116, v116, v117
	v_cvt_pk_bf16_f32 v117, v118, v119
	v_cvt_pk_bf16_f32 v118, v120, v121
	v_cvt_pk_bf16_f32 v119, v122, v123
	global_store_dwordx4 v[132:133], v[116:119], off
	v_pk_mul_f32 v[120:121], v[130:131], v[146:147] op_sel_hi:[1,0]
	v_pk_mul_f32 v[122:123], v[128:129], v[146:147] op_sel_hi:[1,0]
	v_pk_mul_f32 v[118:119], v[126:127], v[146:147] op_sel_hi:[1,0]
	v_pk_mul_f32 v[116:117], v[124:125], v[146:147] op_sel_hi:[1,0]
	s_nop 0
	v_cvt_pk_bf16_f32 v116, v116, v117
	v_cvt_pk_bf16_f32 v117, v118, v119
	v_cvt_pk_bf16_f32 v118, v122, v123
	v_cvt_pk_bf16_f32 v119, v120, v121
	global_store_dwordx4 v[132:133], v[116:119], off offset:256
	s_nop 1
	v_or_b32_e32 v116, 16, v136
	v_ashrrev_i32_e32 v117, 31, v116
	v_lshlrev_b64 v[118:119], 11, v[116:117]
	v_lshl_add_u64 v[116:117], v[116:117], 2, s[2:3]
	s_nop 0
	v_lshl_add_u64 v[118:119], s[8:9], 0, v[118:119]
	v_lshl_add_u64 v[118:119], v[118:119], 0, v[138:139]
	s_nop 0
	v_pk_mul_f32 v[100:101], v[100:101], v[148:149] op_sel_hi:[1,0]
	v_pk_mul_f32 v[98:99], v[98:99], v[148:149] op_sel_hi:[1,0]
	v_pk_mul_f32 v[104:105], v[104:105], v[148:149] op_sel_hi:[1,0]
	v_pk_mul_f32 v[102:103], v[102:103], v[148:149] op_sel_hi:[1,0]
	v_cvt_pk_bf16_f32 v98, v98, v99
	v_cvt_pk_bf16_f32 v99, v100, v101
	v_cvt_pk_bf16_f32 v100, v102, v103
	v_cvt_pk_bf16_f32 v101, v104, v105
	global_store_dwordx4 v[118:119], v[98:101], off
	v_pk_mul_f32 v[102:103], v[112:113], v[148:149] op_sel_hi:[1,0]
	v_pk_mul_f32 v[104:105], v[110:111], v[148:149] op_sel_hi:[1,0]
	v_pk_mul_f32 v[100:101], v[108:109], v[148:149] op_sel_hi:[1,0]
	v_pk_mul_f32 v[98:99], v[106:107], v[148:149] op_sel_hi:[1,0]
	s_nop 0
	v_cvt_pk_bf16_f32 v98, v98, v99
	v_cvt_pk_bf16_f32 v99, v100, v101
	v_cvt_pk_bf16_f32 v100, v104, v105
	v_cvt_pk_bf16_f32 v101, v102, v103
	global_store_dwordx4 v[118:119], v[98:101], off offset:256
	s_nop 1
	v_or_b32_e32 v98, 32, v136
	v_ashrrev_i32_e32 v99, 31, v98
	v_lshlrev_b64 v[100:101], 11, v[98:99]
	v_lshl_add_u64 v[98:99], v[98:99], 2, s[2:3]
	s_nop 0
	v_lshl_add_u64 v[100:101], s[8:9], 0, v[100:101]
	v_lshl_add_u64 v[100:101], v[100:101], 0, v[138:139]
	s_nop 0
	v_pk_mul_f32 v[84:85], v[84:85], v[150:151] op_sel_hi:[1,0]
	v_pk_mul_f32 v[82:83], v[82:83], v[150:151] op_sel_hi:[1,0]
	v_pk_mul_f32 v[88:89], v[88:89], v[150:151] op_sel_hi:[1,0]
	v_pk_mul_f32 v[86:87], v[86:87], v[150:151] op_sel_hi:[1,0]
	v_cvt_pk_bf16_f32 v82, v82, v83
	v_cvt_pk_bf16_f32 v83, v84, v85
	v_cvt_pk_bf16_f32 v84, v86, v87
	v_cvt_pk_bf16_f32 v85, v88, v89
	global_store_dwordx4 v[100:101], v[82:85], off
	v_pk_mul_f32 v[86:87], v[96:97], v[150:151] op_sel_hi:[1,0]
	v_pk_mul_f32 v[88:89], v[94:95], v[150:151] op_sel_hi:[1,0]
	v_pk_mul_f32 v[84:85], v[92:93], v[150:151] op_sel_hi:[1,0]
	v_pk_mul_f32 v[82:83], v[90:91], v[150:151] op_sel_hi:[1,0]
	s_nop 0
	v_cvt_pk_bf16_f32 v82, v82, v83
	v_cvt_pk_bf16_f32 v83, v84, v85
	v_cvt_pk_bf16_f32 v84, v88, v89
	v_cvt_pk_bf16_f32 v85, v86, v87
	global_store_dwordx4 v[100:101], v[82:85], off offset:256
	s_nop 1
	v_or_b32_e32 v82, 48, v136
	v_ashrrev_i32_e32 v83, 31, v82
	v_lshlrev_b64 v[84:85], 11, v[82:83]
	v_lshl_add_u64 v[82:83], v[82:83], 2, s[2:3]
	s_nop 0
	v_lshl_add_u64 v[84:85], s[8:9], 0, v[84:85]
	v_lshl_add_u64 v[84:85], v[84:85], 0, v[138:139]
	s_nop 0
	v_pk_mul_f32 v[80:81], v[80:81], v[152:153] op_sel_hi:[1,0]
	v_pk_mul_f32 v[78:79], v[78:79], v[152:153] op_sel_hi:[1,0]
	v_pk_mul_f32 v[86:87], v[76:77], v[152:153] op_sel_hi:[1,0]
	v_pk_mul_f32 v[76:77], v[74:75], v[152:153] op_sel_hi:[1,0]
	v_cvt_pk_bf16_f32 v74, v78, v79
	v_cvt_pk_bf16_f32 v75, v80, v81
	v_cvt_pk_bf16_f32 v76, v76, v77
	v_cvt_pk_bf16_f32 v77, v86, v87
	global_store_dwordx4 v[84:85], v[74:77], off
	v_pk_mul_f32 v[62:63], v[62:63], v[152:153] op_sel_hi:[1,0]
	v_pk_mul_f32 v[60:61], v[60:61], v[152:153] op_sel_hi:[1,0]
	v_pk_mul_f32 v[74:75], v[58:59], v[152:153] op_sel_hi:[1,0]
	v_pk_mul_f32 v[58:59], v[56:57], v[152:153] op_sel_hi:[1,0]
	v_cvt_pk_bf16_f32 v56, v60, v61
	v_cvt_pk_bf16_f32 v57, v62, v63
	v_cvt_pk_bf16_f32 v58, v58, v59
	v_cvt_pk_bf16_f32 v59, v74, v75
	global_store_dwordx4 v[84:85], v[56:59], off offset:256
	s_nop 0
	v_lshl_add_u64 v[60:61], v[132:133], 0, s[4:5]
	s_mov_b32 s4, 0x40000
	s_nop 0
	v_pk_mul_f32 v[58:59], v[68:69], v[154:155] op_sel_hi:[1,0]
	v_pk_mul_f32 v[56:57], v[66:67], v[154:155] op_sel_hi:[1,0]
	v_pk_mul_f32 v[66:67], v[72:73], v[154:155] op_sel_hi:[1,0]
	v_pk_mul_f32 v[68:69], v[70:71], v[154:155] op_sel_hi:[1,0]
	v_cvt_pk_bf16_f32 v56, v56, v57
	v_cvt_pk_bf16_f32 v57, v58, v59
	v_cvt_pk_bf16_f32 v59, v66, v67
	v_add_co_u32_e32 v66, vcc, s4, v132
	v_cvt_pk_bf16_f32 v58, v68, v69
	s_nop 0
	v_addc_co_u32_e32 v67, vcc, 0, v133, vcc
	global_store_dwordx4 v[66:67], v[56:59], off
	v_pk_mul_f32 v[54:55], v[54:55], v[154:155] op_sel_hi:[1,0]
	v_pk_mul_f32 v[52:53], v[52:53], v[154:155] op_sel_hi:[1,0]
	v_pk_mul_f32 v[56:57], v[50:51], v[154:155] op_sel_hi:[1,0]
	v_pk_mul_f32 v[50:51], v[48:49], v[154:155] op_sel_hi:[1,0]
	v_cvt_pk_bf16_f32 v48, v52, v53
	v_cvt_pk_bf16_f32 v49, v54, v55
	v_cvt_pk_bf16_f32 v50, v50, v51
	v_cvt_pk_bf16_f32 v51, v56, v57
	global_store_dwordx4 v[60:61], v[48:51], off offset:256
	s_nop 0
	s_mov_b64 s[4:5], 0x48000
	v_lshl_add_u64 v[48:49], v[132:133], 0, s[4:5]
	s_mov_b32 s4, 0x48000
	s_nop 0
	v_pk_mul_f32 v[42:43], v[42:43], v[156:157] op_sel_hi:[1,0]
	v_pk_mul_f32 v[40:41], v[40:41], v[156:157] op_sel_hi:[1,0]
	v_pk_mul_f32 v[44:45], v[44:45], v[156:157] op_sel_hi:[1,0]
	v_pk_mul_f32 v[46:47], v[46:47], v[156:157] op_sel_hi:[1,0]
	v_cvt_pk_bf16_f32 v40, v40, v41
	v_cvt_pk_bf16_f32 v41, v42, v43
	v_cvt_pk_bf16_f32 v42, v44, v45
	v_add_co_u32_e32 v44, vcc, s4, v132
	v_cvt_pk_bf16_f32 v43, v46, v47
	s_nop 0
	v_addc_co_u32_e32 v45, vcc, 0, v133, vcc
	global_store_dwordx4 v[44:45], v[40:43], off
	v_pk_mul_f32 v[38:39], v[38:39], v[156:157] op_sel_hi:[1,0]
	v_pk_mul_f32 v[36:37], v[36:37], v[156:157] op_sel_hi:[1,0]
	v_pk_mul_f32 v[40:41], v[34:35], v[156:157] op_sel_hi:[1,0]
	v_pk_mul_f32 v[34:35], v[32:33], v[156:157] op_sel_hi:[1,0]
	v_cvt_pk_bf16_f32 v32, v36, v37
	v_cvt_pk_bf16_f32 v33, v38, v39
	v_cvt_pk_bf16_f32 v34, v34, v35
	v_cvt_pk_bf16_f32 v35, v40, v41
	global_store_dwordx4 v[48:49], v[32:35], off offset:256
	s_nop 0
	s_mov_b64 s[4:5], 0x50000
	v_lshl_add_u64 v[32:33], v[132:133], 0, s[4:5]
	s_mov_b32 s4, 0x50000
	s_nop 0
	v_pk_mul_f32 v[26:27], v[26:27], v[158:159] op_sel_hi:[1,0]
	v_pk_mul_f32 v[24:25], v[24:25], v[158:159] op_sel_hi:[1,0]
	v_pk_mul_f32 v[28:29], v[28:29], v[158:159] op_sel_hi:[1,0]
	v_pk_mul_f32 v[30:31], v[30:31], v[158:159] op_sel_hi:[1,0]
	v_cvt_pk_bf16_f32 v24, v24, v25
	v_cvt_pk_bf16_f32 v25, v26, v27
	v_cvt_pk_bf16_f32 v26, v28, v29
	v_add_co_u32_e32 v28, vcc, s4, v132
	v_cvt_pk_bf16_f32 v27, v30, v31
	s_nop 0
	v_addc_co_u32_e32 v29, vcc, 0, v133, vcc
	global_store_dwordx4 v[28:29], v[24:27], off
	v_pk_mul_f32 v[22:23], v[22:23], v[158:159] op_sel_hi:[1,0]
	v_pk_mul_f32 v[20:21], v[20:21], v[158:159] op_sel_hi:[1,0]
	v_pk_mul_f32 v[24:25], v[18:19], v[158:159] op_sel_hi:[1,0]
	v_pk_mul_f32 v[18:19], v[16:17], v[158:159] op_sel_hi:[1,0]
	v_cvt_pk_bf16_f32 v16, v20, v21
	v_cvt_pk_bf16_f32 v17, v22, v23
	v_cvt_pk_bf16_f32 v18, v18, v19
	v_cvt_pk_bf16_f32 v19, v24, v25
	global_store_dwordx4 v[32:33], v[16:19], off offset:256
	s_nop 0
	s_mov_b64 s[4:5], 0x58000
	v_lshl_add_u64 v[18:19], v[132:133], 0, s[4:5]
	s_mov_b32 s4, 0x58000
	s_nop 0
	v_pk_mul_f32 v[2:3], v[2:3], v[160:161] op_sel_hi:[1,0]
	v_pk_mul_f32 v[0:1], v[0:1], v[160:161] op_sel_hi:[1,0]
	v_pk_mul_f32 v[4:5], v[4:5], v[160:161] op_sel_hi:[1,0]
	v_pk_mul_f32 v[6:7], v[6:7], v[160:161] op_sel_hi:[1,0]
	v_cvt_pk_bf16_f32 v0, v0, v1
	v_cvt_pk_bf16_f32 v1, v2, v3
	v_cvt_pk_bf16_f32 v2, v4, v5
	v_add_co_u32_e32 v4, vcc, s4, v132
	v_cvt_pk_bf16_f32 v3, v6, v7
	s_nop 0
	v_addc_co_u32_e32 v5, vcc, 0, v133, vcc
	global_store_dwordx4 v[4:5], v[0:3], off
	v_pk_mul_f32 v[4:5], v[14:15], v[160:161] op_sel_hi:[1,0]
	v_pk_mul_f32 v[6:7], v[12:13], v[160:161] op_sel_hi:[1,0]
	v_pk_mul_f32 v[2:3], v[10:11], v[160:161] op_sel_hi:[1,0]
	v_pk_mul_f32 v[0:1], v[8:9], v[160:161] op_sel_hi:[1,0]
	s_mov_b64 s[4:5], -1
	v_cvt_pk_bf16_f32 v0, v0, v1
	v_cvt_pk_bf16_f32 v1, v2, v3
	v_cvt_pk_bf16_f32 v2, v6, v7
	v_cvt_pk_bf16_f32 v3, v4, v5
	s_and_b64 vcc, exec, s[0:1]
	global_store_dwordx4 v[18:19], v[0:3], off offset:256
	s_cbranch_vccnz .LBB0_1500
	s_andn2_b64 vcc, exec, s[6:7]
	s_cbranch_vccnz .LBB0_1499
	s_barrier
	s_branch .LBB0_1499
